# attention last dilation group skips its dead LSE store (no reader after g2)
# baseline (speedup 1.0000x reference)
; __device__ __forceinline__ void attn_group_mfma5(const bf16* QK, const float* bias2g, int ldil, int first, bf16* OACC, float* LSE, LAS unsigned char* lds, const int tid, const int bid, const int G) {
;     ...
;         if (kq == 0) LSE[rowq * 16 + h] = lse;
.LBB0_220:
	s_cmp_eq_u32 s24, 2
	s_cbranch_scc1 .LBB0_221
	s_lshl_b32 s60, s0, 13
	v_lshl_add_u64 v[30:31], v[62:63], 0, s[60:61]
	global_store_dword v[30:31], v28, off
